# write-through sc0 sc1 on dwordx4 epilogue stores of in-proj, out-proj, down GEMMs
# baseline (speedup 1.0000x reference)
; __device__ __forceinline__ unsigned cvt_pk_bf16(float lo, float hi) { unsigned r; asm volatile("v_cvt_pk_bf16_f32 %0, %1, %2" : "=v"(r) : "v"(lo), "v"(hi)); return r; }
;     __device__ __forceinline__ void operator()(const f32x4 (&acc)[2][2][4][2], const Unit& u, int wr, int wc, int fr, int fq) const {
;         const int row0 = u.pm * BM + wr * 64 + fr;
;         if (u.pn < 13) {
;             const int col0 = u.pn * BM + wc * 32 + 8 * fq;
; #pragma unroll
;             for (int ai = 0; ai < 2; ++ai)
; #pragma unroll
;                 for (int m = 0; m < 4; ++m) { bf16_t* rowp = P + (size_t)(row0 + ai * HALF + m * 16) * 3328 + col0;
; #pragma unroll
;                     for (int bj = 0; bj < 2; ++bj) { const f32x4 v0 = acc[ai][bj][m][0], v1 = acc[ai][bj][m][1];
;                         u32x4 w; w.x = cvt_pk_bf16(v0[0], v0[1]); w.y = cvt_pk_bf16(v0[2], v0[3]); w.z = cvt_pk_bf16(v1[0], v1[1]); w.w = cvt_pk_bf16(v1[2], v1[3]);
;                         *(u32x4*)(rowp + bj * HALF) = w; } }
.LBB0_768:
	v_lshl_or_b32 v148, s72, 8, v151
	v_ashrrev_i32_e32 v149, 31, v148
	v_mov_b64_e32 v[146:147], s[6:7]
	v_mad_i64_i32 v[154:155], s[20:21], v144, s33, v[146:147]
	v_lshlrev_b64 v[148:149], 1, v[148:149]
	v_lshl_add_u64 v[154:155], v[154:155], 0, v[148:149]
	v_or_b32_e32 v0, 16, v144
	v_cvt_pk_bf16_f32 v128, v128, v129
	v_cvt_pk_bf16_f32 v129, v130, v131
	v_cvt_pk_bf16_f32 v130, v124, v125
	v_cvt_pk_bf16_f32 v131, v126, v127
	global_store_dwordx4 v[154:155], v[128:131], off sc0 sc1
	v_cvt_pk_bf16_f32 v116, v116, v117
	v_cvt_pk_bf16_f32 v117, v118, v119
	v_cvt_pk_bf16_f32 v118, v108, v109
	v_mad_i64_i32 v[108:109], s[20:21], v0, s33, v[146:147]
	v_cvt_pk_bf16_f32 v119, v110, v111
	global_store_dwordx4 v[154:155], v[116:119], off offset:256 sc0 sc1
	v_or_b32_e32 v0, 32, v144
	s_nop 0
	v_lshl_add_u64 v[116:117], v[108:109], 0, v[148:149]
	v_cvt_pk_bf16_f32 v108, v120, v121
	v_cvt_pk_bf16_f32 v109, v122, v123
	v_cvt_pk_bf16_f32 v110, v112, v113
	v_cvt_pk_bf16_f32 v111, v114, v115
	global_store_dwordx4 v[116:117], v[108:111], off sc0 sc1
	v_cvt_pk_bf16_f32 v100, v100, v101
	v_cvt_pk_bf16_f32 v101, v102, v103
	v_cvt_pk_bf16_f32 v102, v92, v93
	v_mad_i64_i32 v[92:93], s[20:21], v0, s33, v[146:147]
	v_cvt_pk_bf16_f32 v103, v94, v95
	global_store_dwordx4 v[116:117], v[100:103], off offset:256 sc0 sc1
	v_or_b32_e32 v0, 48, v144
	s_nop 0
	v_lshl_add_u64 v[100:101], v[92:93], 0, v[148:149]
	v_cvt_pk_bf16_f32 v92, v104, v105
	v_cvt_pk_bf16_f32 v93, v106, v107
	v_cvt_pk_bf16_f32 v94, v96, v97
	v_cvt_pk_bf16_f32 v95, v98, v99
	global_store_dwordx4 v[100:101], v[92:95], off sc0 sc1
	v_cvt_pk_bf16_f32 v84, v84, v85
	v_cvt_pk_bf16_f32 v85, v86, v87
	v_cvt_pk_bf16_f32 v86, v76, v77
	v_mad_i64_i32 v[76:77], s[20:21], v0, s33, v[146:147]
	v_cvt_pk_bf16_f32 v87, v78, v79
	global_store_dwordx4 v[100:101], v[84:87], off offset:256 sc0 sc1
	v_add_u32_e32 v0, 0x80, v144
	s_nop 0
	v_lshl_add_u64 v[84:85], v[76:77], 0, v[148:149]
	v_cvt_pk_bf16_f32 v76, v88, v89
	v_cvt_pk_bf16_f32 v77, v90, v91
	v_cvt_pk_bf16_f32 v78, v80, v81
	v_cvt_pk_bf16_f32 v79, v82, v83
	global_store_dwordx4 v[84:85], v[76:79], off sc0 sc1
	v_cvt_pk_bf16_f32 v72, v72, v73
	v_cvt_pk_bf16_f32 v73, v74, v75
	v_cvt_pk_bf16_f32 v74, v68, v69
	v_mad_i64_i32 v[68:69], s[20:21], v0, s33, v[146:147]
	v_lshl_add_u64 v[68:69], v[68:69], 0, v[148:149]
	v_add_u32_e32 v0, 0x90, v144
	v_cvt_pk_bf16_f32 v75, v70, v71
	global_store_dwordx4 v[84:85], v[72:75], off offset:256 sc0 sc1
	v_cvt_pk_bf16_f32 v64, v64, v65
	v_cvt_pk_bf16_f32 v65, v66, v67
	v_cvt_pk_bf16_f32 v66, v60, v61
	v_cvt_pk_bf16_f32 v67, v62, v63
	global_store_dwordx4 v[68:69], v[64:67], off sc0 sc1
	v_cvt_pk_bf16_f32 v52, v52, v53
	v_cvt_pk_bf16_f32 v53, v54, v55
	v_cvt_pk_bf16_f32 v54, v44, v45
	v_mad_i64_i32 v[44:45], s[20:21], v0, s33, v[146:147]
	v_cvt_pk_bf16_f32 v55, v46, v47
	global_store_dwordx4 v[68:69], v[52:55], off offset:256 sc0 sc1
	v_add_u32_e32 v0, 0xa0, v144
	s_nop 0
	v_lshl_add_u64 v[52:53], v[44:45], 0, v[148:149]
	v_cvt_pk_bf16_f32 v44, v56, v57
	v_cvt_pk_bf16_f32 v45, v58, v59
	v_cvt_pk_bf16_f32 v46, v48, v49
	v_cvt_pk_bf16_f32 v47, v50, v51
	global_store_dwordx4 v[52:53], v[44:47], off sc0 sc1
	v_cvt_pk_bf16_f32 v36, v36, v37
	v_cvt_pk_bf16_f32 v37, v38, v39
	v_cvt_pk_bf16_f32 v38, v28, v29
	v_mad_i64_i32 v[28:29], s[20:21], v0, s33, v[146:147]
	v_cvt_pk_bf16_f32 v39, v30, v31
	global_store_dwordx4 v[52:53], v[36:39], off offset:256 sc0 sc1
	v_add_u32_e32 v0, 0xb0, v144
	s_nop 0
	v_lshl_add_u64 v[36:37], v[28:29], 0, v[148:149]
	v_cvt_pk_bf16_f32 v28, v40, v41
	v_cvt_pk_bf16_f32 v29, v42, v43
	v_cvt_pk_bf16_f32 v30, v32, v33
	v_cvt_pk_bf16_f32 v31, v34, v35
	global_store_dwordx4 v[36:37], v[28:31], off sc0 sc1
	v_cvt_pk_bf16_f32 v20, v20, v21
	v_cvt_pk_bf16_f32 v21, v22, v23
	v_cvt_pk_bf16_f32 v22, v12, v13
	v_mad_i64_i32 v[12:13], s[20:21], v0, s33, v[146:147]
	v_cvt_pk_bf16_f32 v23, v14, v15
	global_store_dwordx4 v[36:37], v[20:23], off offset:256 sc0 sc1
	s_nop 1
	v_lshl_add_u64 v[20:21], v[12:13], 0, v[148:149]
	v_cvt_pk_bf16_f32 v12, v24, v25
	v_cvt_pk_bf16_f32 v13, v26, v27
	v_cvt_pk_bf16_f32 v14, v16, v17
	v_cvt_pk_bf16_f32 v15, v18, v19
	global_store_dwordx4 v[20:21], v[12:15], off sc0 sc1
	v_cvt_pk_bf16_f32 v8, v8, v9
	v_cvt_pk_bf16_f32 v9, v10, v11
	v_cvt_pk_bf16_f32 v10, v4, v5
	v_cvt_pk_bf16_f32 v11, v6, v7
	global_store_dwordx4 v[20:21], v[8:11], off offset:256 sc0 sc1
	s_andn2_b64 vcc, exec, s[2:3]
	s_mov_b64 s[2:3], -1
	s_cbranch_vccnz .LBB0_760
	s_branch .LBB0_774

;     __device__ __forceinline__ void operator()(const f32x4 (&acc)[2][2][4][2], const Unit& u, int wr, int wc, int fr, int fq) const {
;     ...
;         } else if (wc == 0 && fq < 2) {
; #pragma unroll
;             for (int ai = 0; ai < 2; ++ai)
; #pragma unroll
;                 for (int m = 0; m < 4; ++m) { float* gp = G + (size_t)(row0 + ai * HALF + m * 16) * 16 + 8 * fq;
;                     *(f32x4*)(gp) = acc[ai][0][m][0]; *(f32x4*)(gp + 4) = acc[ai][0][m][1]; }
.LBB0_770:
	s_and_saveexec_b64 s[20:21], s[12:13]
	s_cbranch_execz .LBB0_772
	v_or_b32_e32 v148, 16, v144
	v_ashrrev_i32_e32 v145, 31, v144
	v_ashrrev_i32_e32 v149, 31, v148
	v_lshlrev_b64 v[146:147], 6, v[144:145]
	v_lshlrev_b64 v[148:149], 6, v[148:149]
	v_lshl_add_u64 v[146:147], v[138:139], 0, v[146:147]
	v_lshl_add_u64 v[148:149], v[138:139], 0, v[148:149]
	global_store_dwordx4 v[146:147], v[128:131], off sc0 sc1
	global_store_dwordx4 v[146:147], v[124:127], off offset:16 sc0 sc1
	global_store_dwordx4 v[148:149], v[120:123], off sc0 sc1
	global_store_dwordx4 v[148:149], v[112:115], off offset:16 sc0 sc1
	v_or_b32_e32 v148, 32, v144
	v_ashrrev_i32_e32 v149, 31, v148
	v_lshlrev_b64 v[148:149], 6, v[148:149]
	v_lshl_add_u64 v[148:149], v[138:139], 0, v[148:149]
	global_store_dwordx4 v[148:149], v[104:107], off sc0 sc1
	global_store_dwordx4 v[148:149], v[96:99], off offset:16 sc0 sc1
	v_or_b32_e32 v148, 48, v144
	v_ashrrev_i32_e32 v149, 31, v148
	v_lshlrev_b64 v[148:149], 6, v[148:149]
	v_lshl_add_u64 v[148:149], v[138:139], 0, v[148:149]
	s_mov_b64 s[22:23], 0x2000
	v_add_co_u32_e32 v154, vcc, 0x2000, v146
	global_store_dwordx4 v[148:149], v[88:91], off sc0 sc1
	global_store_dwordx4 v[148:149], v[80:83], off offset:16 sc0 sc1
	v_lshl_add_u64 v[148:149], v[146:147], 0, s[22:23]
	v_addc_co_u32_e32 v155, vcc, 0, v147, vcc
	s_mov_b64 s[22:23], 0x2400
	global_store_dwordx4 v[154:155], v[64:67], off sc0 sc1
	global_store_dwordx4 v[148:149], v[60:63], off offset:16 sc0 sc1
	v_lshl_add_u64 v[148:149], v[146:147], 0, s[22:23]
	s_mov_b64 s[22:23], 0x2800
	global_store_dwordx4 v[154:155], v[56:59], off offset:1024 sc0 sc1
	global_store_dwordx4 v[148:149], v[48:51], off offset:16 sc0 sc1
	v_lshl_add_u64 v[148:149], v[146:147], 0, s[22:23]
	s_mov_b64 s[22:23], 0x2c00
	global_store_dwordx4 v[154:155], v[40:43], off offset:2048 sc0 sc1
	global_store_dwordx4 v[148:149], v[32:35], off offset:16 sc0 sc1
	v_lshl_add_u64 v[146:147], v[146:147], 0, s[22:23]
	global_store_dwordx4 v[154:155], v[24:27], off offset:3072 sc0 sc1
	global_store_dwordx4 v[146:147], v[16:19], off offset:16 sc0 sc1

; __device__ __forceinline__ unsigned cvt_pk_bf16(float lo, float hi) { unsigned r; asm volatile("v_cvt_pk_bf16_f32 %0, %1, %2" : "=v"(r) : "v"(lo), "v"(hi)); return r; }
;     __device__ __forceinline__ void operator()(const f32x4 (&acc)[2][2][4][2], const Unit& u, int wr, int wc, int fr, int fq) const {
;         const int row0 = u.pm * BM + wr * 64 + fr, col0 = u.pn * BM + wc * 32 + 8 * fq;
;         const float* gb = gate + (size_t)((u.pm * BM) >> 13) * 6144 + col0;
;         f32x4 gv[2][2];
; #pragma unroll
;         for (int bj = 0; bj < 2; ++bj)
; #pragma unroll
;             for (int n = 0; n < 2; ++n) gv[bj][n] = *(const f32x4*)(gb + bj * HALF + n * 4);
; #pragma unroll
;         for (int ai = 0; ai < 2; ++ai)
; #pragma unroll
;             for (int m = 0; m < 4; ++m) { bf16_t* rowp = X + (size_t)(row0 + ai * HALF + m * 16) * 1024 + col0;
; #pragma unroll
;                 for (int bj = 0; bj < 2; ++bj) { const u32x4 xr = *(const u32x4*)(rowp + bj * HALF);
;                     f32x4 x0, x1; x0[0] = __uint_as_float(xr.x << 16); x0[1] = __uint_as_float(xr.x & 0xffff0000u); x0[2] = __uint_as_float(xr.y << 16); x0[3] = __uint_as_float(xr.y & 0xffff0000u);
;                     x1[0] = __uint_as_float(xr.z << 16); x1[1] = __uint_as_float(xr.z & 0xffff0000u); x1[2] = __uint_as_float(xr.w << 16); x1[3] = __uint_as_float(xr.w & 0xffff0000u);
;                     x0 = x0 + gv[bj][0] * acc[ai][bj][m][0]; x1 = x1 + gv[bj][1] * acc[ai][bj][m][1];
;                     u32x4 w; w.x = cvt_pk_bf16(x0[0], x0[1]); w.y = cvt_pk_bf16(x0[2], x0[3]); w.z = cvt_pk_bf16(x1[0], x1[1]); w.w = cvt_pk_bf16(x1[2], x1[3]);
;                     *(u32x4*)(rowp + bj * HALF) = w; } }
.LBB0_3171:
	v_lshl_add_u32 v160, s18, 8, v1
	v_lshl_or_b32 v116, s62, 8, v165
	v_ashrrev_i32_e32 v161, 31, v160
	v_ashrrev_i32_e32 v117, 31, v116
	v_lshlrev_b64 v[118:119], 11, v[160:161]
	v_lshl_add_u64 v[118:119], s[6:7], 0, v[118:119]
	v_lshlrev_b64 v[162:163], 1, v[116:117]
	s_ashr_i32 s11, s18, 5
	v_lshl_add_u64 v[158:159], v[118:119], 0, v[162:163]
	s_mul_hi_i32 s13, s11, 0x6000
	s_mulk_i32 s11, 0x6000
	global_load_dwordx4 v[168:171], v[158:159], off
	s_add_u32 s20, s44, s11
	s_addc_u32 s21, s45, s13
	v_lshl_add_u64 v[120:121], v[116:117], 2, s[20:21]
	global_load_dwordx4 v[136:139], v[120:121], off
	global_load_dwordx4 v[132:135], v[120:121], off offset:16
	global_load_dwordx4 v[116:119], v[120:121], off offset:528
	s_nop 0
	global_load_dwordx4 v[120:123], v[120:121], off offset:512
	s_mov_b32 s11, 0x40000
	s_mov_b64 s[20:21], 0x40000
	s_waitcnt vmcnt(0)
	v_lshlrev_b32_e32 v172, 16, v168
	v_and_b32_e32 v173, 0xffff0000, v168
	v_lshlrev_b32_e32 v168, 16, v169
	v_and_b32_e32 v169, 0xffff0000, v169
	v_lshlrev_b32_e32 v174, 16, v170
	v_and_b32_e32 v175, 0xffff0000, v170
	v_lshlrev_b32_e32 v170, 16, v171
	v_and_b32_e32 v171, 0xffff0000, v171
	v_pk_fma_f32 v[146:147], v[146:147], v[138:139], v[168:169]
	v_pk_fma_f32 v[144:145], v[144:145], v[136:137], v[172:173]
	v_pk_fma_f32 v[168:169], v[142:143], v[134:135], v[170:171]
	v_pk_fma_f32 v[142:143], v[140:141], v[132:133], v[174:175]
	v_cvt_pk_bf16_f32 v140, v144, v145
	v_cvt_pk_bf16_f32 v141, v146, v147
	s_nop 0
	v_cvt_pk_bf16_f32 v142, v142, v143
	v_cvt_pk_bf16_f32 v143, v168, v169
	global_load_dwordx4 v[144:147], v[158:159], off offset:256
	v_or_b32_e32 v168, 16, v160
	v_ashrrev_i32_e32 v169, 31, v168
	v_lshlrev_b64 v[168:169], 11, v[168:169]
	v_lshl_add_u64 v[168:169], s[6:7], 0, v[168:169]
	global_store_dwordx4 v[158:159], v[140:143], off sc0 sc1
	v_lshl_add_u64 v[168:169], v[168:169], 0, v[162:163]
	s_waitcnt vmcnt(1)
	v_lshlrev_b32_e32 v140, 16, v144
	v_and_b32_e32 v141, 0xffff0000, v144
	v_lshlrev_b32_e32 v142, 16, v145
	v_and_b32_e32 v143, 0xffff0000, v145
	v_lshlrev_b32_e32 v144, 16, v146
	v_and_b32_e32 v145, 0xffff0000, v146
	v_lshlrev_b32_e32 v146, 16, v147
	v_and_b32_e32 v147, 0xffff0000, v147
	v_pk_fma_f32 v[126:127], v[126:127], v[122:123], v[142:143]
	v_pk_fma_f32 v[124:125], v[124:125], v[120:121], v[140:141]
	v_pk_fma_f32 v[140:141], v[114:115], v[118:119], v[146:147]
	v_pk_fma_f32 v[114:115], v[112:113], v[116:117], v[144:145]
	v_cvt_pk_bf16_f32 v112, v124, v125
	v_cvt_pk_bf16_f32 v113, v126, v127
	s_nop 0
	v_cvt_pk_bf16_f32 v114, v114, v115
	v_cvt_pk_bf16_f32 v115, v140, v141
	global_load_dwordx4 v[124:127], v[168:169], off
	s_nop 0
	global_store_dwordx4 v[158:159], v[112:115], off offset:256 sc0 sc1
	s_waitcnt vmcnt(1)
	s_nop 0
	v_lshlrev_b32_e32 v112, 16, v124
	v_and_b32_e32 v113, 0xffff0000, v124
	v_lshlrev_b32_e32 v114, 16, v125
	v_and_b32_e32 v115, 0xffff0000, v125
	v_lshlrev_b32_e32 v124, 16, v126
	v_and_b32_e32 v125, 0xffff0000, v126
	v_lshlrev_b32_e32 v126, 16, v127
	v_and_b32_e32 v127, 0xffff0000, v127
	v_pk_fma_f32 v[114:115], v[130:131], v[138:139], v[114:115]
	v_pk_fma_f32 v[112:113], v[128:129], v[136:137], v[112:113]
	v_pk_fma_f32 v[126:127], v[110:111], v[134:135], v[126:127]
	v_pk_fma_f32 v[110:111], v[108:109], v[132:133], v[124:125]
	v_cvt_pk_bf16_f32 v108, v112, v113
	v_cvt_pk_bf16_f32 v109, v114, v115
	v_or_b32_e32 v124, 32, v160
	v_cvt_pk_bf16_f32 v110, v110, v111
	v_cvt_pk_bf16_f32 v111, v126, v127
	global_load_dwordx4 v[112:115], v[168:169], off offset:256
	v_ashrrev_i32_e32 v125, 31, v124
	v_lshlrev_b64 v[124:125], 11, v[124:125]
	v_lshl_add_u64 v[124:125], s[6:7], 0, v[124:125]
	global_store_dwordx4 v[168:169], v[108:111], off sc0 sc1
	v_lshl_add_u64 v[124:125], v[124:125], 0, v[162:163]
	s_waitcnt vmcnt(1)
	v_lshlrev_b32_e32 v108, 16, v112
	v_and_b32_e32 v109, 0xffff0000, v112
	v_lshlrev_b32_e32 v110, 16, v113
	v_and_b32_e32 v111, 0xffff0000, v113
	v_lshlrev_b32_e32 v112, 16, v114
	v_and_b32_e32 v113, 0xffff0000, v114
	v_lshlrev_b32_e32 v114, 16, v115
	v_and_b32_e32 v115, 0xffff0000, v115
	v_pk_fma_f32 v[102:103], v[102:103], v[122:123], v[110:111]
	v_pk_fma_f32 v[100:101], v[100:101], v[120:121], v[108:109]
	v_pk_fma_f32 v[108:109], v[98:99], v[118:119], v[114:115]
	v_pk_fma_f32 v[98:99], v[96:97], v[116:117], v[112:113]
	v_cvt_pk_bf16_f32 v96, v100, v101
	v_cvt_pk_bf16_f32 v97, v102, v103
	s_nop 0
	v_cvt_pk_bf16_f32 v98, v98, v99
	v_cvt_pk_bf16_f32 v99, v108, v109
	global_load_dwordx4 v[100:103], v[124:125], off
	s_nop 0
	global_store_dwordx4 v[168:169], v[96:99], off offset:256 sc0 sc1
	s_waitcnt vmcnt(1)
	s_nop 0
	v_lshlrev_b32_e32 v96, 16, v100
	v_and_b32_e32 v97, 0xffff0000, v100
	v_lshlrev_b32_e32 v98, 16, v101
	v_and_b32_e32 v99, 0xffff0000, v101
	v_lshlrev_b32_e32 v100, 16, v102
	v_and_b32_e32 v101, 0xffff0000, v102
	v_lshlrev_b32_e32 v102, 16, v103
	v_and_b32_e32 v103, 0xffff0000, v103
	v_pk_fma_f32 v[98:99], v[106:107], v[138:139], v[98:99]
	v_pk_fma_f32 v[96:97], v[104:105], v[136:137], v[96:97]
	v_pk_fma_f32 v[102:103], v[94:95], v[134:135], v[102:103]
	v_pk_fma_f32 v[94:95], v[92:93], v[132:133], v[100:101]
	v_cvt_pk_bf16_f32 v92, v96, v97
	v_cvt_pk_bf16_f32 v93, v98, v99
	v_or_b32_e32 v100, 48, v160
	v_cvt_pk_bf16_f32 v94, v94, v95
	v_cvt_pk_bf16_f32 v95, v102, v103
	global_load_dwordx4 v[96:99], v[124:125], off offset:256
	v_ashrrev_i32_e32 v101, 31, v100
	v_lshlrev_b64 v[100:101], 11, v[100:101]
	v_lshl_add_u64 v[100:101], s[6:7], 0, v[100:101]
	global_store_dwordx4 v[124:125], v[92:95], off sc0 sc1
	v_lshl_add_u64 v[100:101], v[100:101], 0, v[162:163]
	s_waitcnt vmcnt(1)
; __device__ __forceinline__ unsigned cvt_pk_bf16(float lo, float hi) { unsigned r; asm volatile("v_cvt_pk_bf16_f32 %0, %1, %2" : "=v"(r) : "v"(lo), "v"(hi)); return r; }
;     __device__ __forceinline__ void operator()(const f32x4 (&acc)[2][2][4][2], const Unit& u, int wr, int wc, int fr, int fq) const {
;         const int row0 = u.pm * BM + wr * 64 + fr, col0 = u.pn * BM + wc * 32 + 8 * fq;
;         const float* gb = gate + (size_t)((u.pm * BM) >> 13) * 6144 + col0;
;         f32x4 gv[2][2];
; #pragma unroll
;         for (int bj = 0; bj < 2; ++bj)
; #pragma unroll
;             for (int n = 0; n < 2; ++n) gv[bj][n] = *(const f32x4*)(gb + bj * HALF + n * 4);
; #pragma unroll
;         for (int ai = 0; ai < 2; ++ai)
; #pragma unroll
;             for (int m = 0; m < 4; ++m) { bf16_t* rowp = X + (size_t)(row0 + ai * HALF + m * 16) * 1024 + col0;
; #pragma unroll
;                 for (int bj = 0; bj < 2; ++bj) { const u32x4 xr = *(const u32x4*)(rowp + bj * HALF);
;                     f32x4 x0, x1; x0[0] = __uint_as_float(xr.x << 16); x0[1] = __uint_as_float(xr.x & 0xffff0000u); x0[2] = __uint_as_float(xr.y << 16); x0[3] = __uint_as_float(xr.y & 0xffff0000u);
;                     x1[0] = __uint_as_float(xr.z << 16); x1[1] = __uint_as_float(xr.z & 0xffff0000u); x1[2] = __uint_as_float(xr.w << 16); x1[3] = __uint_as_float(xr.w & 0xffff0000u);
;                     x0 = x0 + gv[bj][0] * acc[ai][bj][m][0]; x1 = x1 + gv[bj][1] * acc[ai][bj][m][1];
;                     u32x4 w; w.x = cvt_pk_bf16(x0[0], x0[1]); w.y = cvt_pk_bf16(x0[2], x0[3]); w.z = cvt_pk_bf16(x1[0], x1[1]); w.w = cvt_pk_bf16(x1[2], x1[3]);
;                     *(u32x4*)(rowp + bj * HALF) = w; } }
	v_lshlrev_b32_e32 v92, 16, v96
	v_and_b32_e32 v93, 0xffff0000, v96
	v_lshlrev_b32_e32 v94, 16, v97
	v_and_b32_e32 v95, 0xffff0000, v97
	v_lshlrev_b32_e32 v96, 16, v98
	v_and_b32_e32 v97, 0xffff0000, v98
	v_lshlrev_b32_e32 v98, 16, v99
	v_and_b32_e32 v99, 0xffff0000, v99
	v_pk_fma_f32 v[86:87], v[86:87], v[122:123], v[94:95]
	v_pk_fma_f32 v[84:85], v[84:85], v[120:121], v[92:93]
	v_pk_fma_f32 v[92:93], v[82:83], v[118:119], v[98:99]
	v_pk_fma_f32 v[82:83], v[80:81], v[116:117], v[96:97]
	v_cvt_pk_bf16_f32 v80, v84, v85
	v_cvt_pk_bf16_f32 v81, v86, v87
	s_nop 0
	v_cvt_pk_bf16_f32 v82, v82, v83
	v_cvt_pk_bf16_f32 v83, v92, v93
	global_load_dwordx4 v[84:87], v[100:101], off
	s_nop 0
	global_store_dwordx4 v[124:125], v[80:83], off offset:256 sc0 sc1
	s_waitcnt vmcnt(1)
	s_nop 0
	v_lshlrev_b32_e32 v80, 16, v84
	v_and_b32_e32 v81, 0xffff0000, v84
	v_lshlrev_b32_e32 v82, 16, v85
	v_and_b32_e32 v83, 0xffff0000, v85
	v_lshlrev_b32_e32 v84, 16, v86
	v_and_b32_e32 v85, 0xffff0000, v86
	v_lshlrev_b32_e32 v86, 16, v87
	v_and_b32_e32 v87, 0xffff0000, v87
	v_pk_fma_f32 v[82:83], v[90:91], v[138:139], v[82:83]
	v_pk_fma_f32 v[80:81], v[88:89], v[136:137], v[80:81]
	v_pk_fma_f32 v[86:87], v[78:79], v[134:135], v[86:87]
	v_pk_fma_f32 v[78:79], v[76:77], v[132:133], v[84:85]
	v_cvt_pk_bf16_f32 v76, v80, v81
	v_cvt_pk_bf16_f32 v77, v82, v83
	v_add_co_u32_e32 v84, vcc, s11, v158
	v_cvt_pk_bf16_f32 v78, v78, v79
	v_cvt_pk_bf16_f32 v79, v86, v87
	global_load_dwordx4 v[80:83], v[100:101], off offset:256
	s_nop 0
	v_addc_co_u32_e32 v85, vcc, 0, v159, vcc
	global_store_dwordx4 v[100:101], v[76:79], off sc0 sc1
	s_mov_b32 s11, 0x48000
	s_waitcnt vmcnt(1)
	v_lshlrev_b32_e32 v76, 16, v80
	v_and_b32_e32 v77, 0xffff0000, v80
	v_lshlrev_b32_e32 v78, 16, v81
	v_and_b32_e32 v79, 0xffff0000, v81
	v_lshlrev_b32_e32 v80, 16, v82
	v_and_b32_e32 v81, 0xffff0000, v82
	v_lshlrev_b32_e32 v82, 16, v83
	v_and_b32_e32 v83, 0xffff0000, v83
	v_pk_fma_f32 v[74:75], v[74:75], v[122:123], v[78:79]
	v_pk_fma_f32 v[72:73], v[72:73], v[120:121], v[76:77]
	v_pk_fma_f32 v[76:77], v[70:71], v[118:119], v[82:83]
	v_pk_fma_f32 v[70:71], v[68:69], v[116:117], v[80:81]
	v_cvt_pk_bf16_f32 v68, v72, v73
	v_cvt_pk_bf16_f32 v69, v74, v75
	s_nop 0
	v_cvt_pk_bf16_f32 v70, v70, v71
	v_cvt_pk_bf16_f32 v71, v76, v77
	global_load_dwordx4 v[72:75], v[84:85], off
	v_lshl_add_u64 v[76:77], v[158:159], 0, s[20:21]
	global_store_dwordx4 v[100:101], v[68:71], off offset:256 sc0 sc1
	s_mov_b64 s[20:21], 0x48000
	s_waitcnt vmcnt(1)
	v_lshlrev_b32_e32 v68, 16, v72
	v_and_b32_e32 v69, 0xffff0000, v72
	v_lshlrev_b32_e32 v70, 16, v73
	v_and_b32_e32 v71, 0xffff0000, v73
	v_lshlrev_b32_e32 v72, 16, v74
	v_and_b32_e32 v73, 0xffff0000, v74
	v_lshlrev_b32_e32 v74, 16, v75
	v_and_b32_e32 v75, 0xffff0000, v75
	v_pk_fma_f32 v[66:67], v[66:67], v[138:139], v[70:71]
	v_pk_fma_f32 v[64:65], v[64:65], v[136:137], v[68:69]
	v_pk_fma_f32 v[68:69], v[62:63], v[134:135], v[74:75]
	v_pk_fma_f32 v[62:63], v[60:61], v[132:133], v[72:73]
	v_cvt_pk_bf16_f32 v60, v64, v65
	v_cvt_pk_bf16_f32 v61, v66, v67
	s_nop 0
	v_cvt_pk_bf16_f32 v62, v62, v63
	v_cvt_pk_bf16_f32 v63, v68, v69
	global_load_dwordx4 v[64:67], v[76:77], off offset:256
	v_add_co_u32_e32 v68, vcc, s11, v158
	global_store_dwordx4 v[84:85], v[60:63], off sc0 sc1
	s_nop 0
	v_addc_co_u32_e32 v69, vcc, 0, v159, vcc
	s_mov_b32 s11, 0x50000
	s_waitcnt vmcnt(1)
	v_lshlrev_b32_e32 v60, 16, v64
	v_and_b32_e32 v61, 0xffff0000, v64
	v_lshlrev_b32_e32 v62, 16, v65
	v_and_b32_e32 v63, 0xffff0000, v65
	v_lshlrev_b32_e32 v64, 16, v66
	v_and_b32_e32 v65, 0xffff0000, v66
	v_lshlrev_b32_e32 v66, 16, v67
	v_and_b32_e32 v67, 0xffff0000, v67
	v_pk_fma_f32 v[58:59], v[58:59], v[122:123], v[62:63]
	v_pk_fma_f32 v[56:57], v[56:57], v[120:121], v[60:61]
	v_pk_fma_f32 v[60:61], v[50:51], v[118:119], v[66:67]
	v_pk_fma_f32 v[50:51], v[48:49], v[116:117], v[64:65]
	v_cvt_pk_bf16_f32 v48, v56, v57
	v_cvt_pk_bf16_f32 v49, v58, v59
	s_nop 0
	v_cvt_pk_bf16_f32 v50, v50, v51
	v_cvt_pk_bf16_f32 v51, v60, v61
	global_load_dwordx4 v[56:59], v[68:69], off
	v_lshl_add_u64 v[60:61], v[158:159], 0, s[20:21]
	global_store_dwordx4 v[76:77], v[48:51], off offset:256 sc0 sc1
	s_mov_b64 s[20:21], 0x50000
	s_waitcnt vmcnt(1)
; __device__ __forceinline__ unsigned cvt_pk_bf16(float lo, float hi) { unsigned r; asm volatile("v_cvt_pk_bf16_f32 %0, %1, %2" : "=v"(r) : "v"(lo), "v"(hi)); return r; }
; template <class Epi, class Sched, bool ALIGN_EPI = false, bool SP2 = false, bool GATHER = false>
; __device__ __forceinline__ void gemm_phase(PG8_LAS unsigned char* lds, const Gemm g, const Sched& S, const Epi& E, const PG8_LAS int* rt = nullptr) {
;     ...
;         if (!has_next) break;
; #pragma unroll
;         for (int a = 0; a < 2; ++a)
; #pragma unroll
;             for (int b = 0; b < 2; ++b)
; #pragma unroll
;                 for (int m = 0; m < 4; ++m)
; #pragma unroll
;                     for (int n = 0; n < 2; ++n) acc[a][b][m][n] = (f32x4){0.f, 0.f, 0.f, 0.f};
;         cur = nxt; cA = nA; cB = nB; ++ui;
;         if constexpr (ALIGN_EPI) { if (wr == 1) PG8_BAR; }
;     __device__ __forceinline__ void operator()(const f32x4 (&acc)[2][2][4][2], const Unit& u, int wr, int wc, int fr, int fq) const {
;         const int row0 = u.pm * BM + wr * 64 + fr, col0 = u.pn * BM + wc * 32 + 8 * fq;
;         const float* gb = gate + (size_t)((u.pm * BM) >> 13) * 6144 + col0;
;         f32x4 gv[2][2];
; #pragma unroll
;         for (int bj = 0; bj < 2; ++bj)
; #pragma unroll
;             for (int n = 0; n < 2; ++n) gv[bj][n] = *(const f32x4*)(gb + bj * HALF + n * 4);
; #pragma unroll
;         for (int ai = 0; ai < 2; ++ai)
; #pragma unroll
;             for (int m = 0; m < 4; ++m) { bf16_t* rowp = X + (size_t)(row0 + ai * HALF + m * 16) * 1024 + col0;
; #pragma unroll
;                 for (int bj = 0; bj < 2; ++bj) { const u32x4 xr = *(const u32x4*)(rowp + bj * HALF);
;                     f32x4 x0, x1; x0[0] = __uint_as_float(xr.x << 16); x0[1] = __uint_as_float(xr.x & 0xffff0000u); x0[2] = __uint_as_float(xr.y << 16); x0[3] = __uint_as_float(xr.y & 0xffff0000u);
;                     x1[0] = __uint_as_float(xr.z << 16); x1[1] = __uint_as_float(xr.z & 0xffff0000u); x1[2] = __uint_as_float(xr.w << 16); x1[3] = __uint_as_float(xr.w & 0xffff0000u);
;                     x0 = x0 + gv[bj][0] * acc[ai][bj][m][0]; x1 = x1 + gv[bj][1] * acc[ai][bj][m][1];
;                     u32x4 w; w.x = cvt_pk_bf16(x0[0], x0[1]); w.y = cvt_pk_bf16(x0[2], x0[3]); w.z = cvt_pk_bf16(x1[0], x1[1]); w.w = cvt_pk_bf16(x1[2], x1[3]);
;                     *(u32x4*)(rowp + bj * HALF) = w; } }
	v_lshlrev_b32_e32 v48, 16, v56
	v_and_b32_e32 v49, 0xffff0000, v56
	v_lshlrev_b32_e32 v50, 16, v57
	v_and_b32_e32 v51, 0xffff0000, v57
	v_lshlrev_b32_e32 v56, 16, v58
	v_and_b32_e32 v57, 0xffff0000, v58
	v_lshlrev_b32_e32 v58, 16, v59
	v_and_b32_e32 v59, 0xffff0000, v59
	v_pk_fma_f32 v[50:51], v[54:55], v[138:139], v[50:51]
	v_pk_fma_f32 v[48:49], v[52:53], v[136:137], v[48:49]
	v_pk_fma_f32 v[52:53], v[46:47], v[134:135], v[58:59]
	v_pk_fma_f32 v[46:47], v[44:45], v[132:133], v[56:57]
	v_cvt_pk_bf16_f32 v44, v48, v49
	v_cvt_pk_bf16_f32 v45, v50, v51
	s_nop 0
	v_cvt_pk_bf16_f32 v46, v46, v47
	v_cvt_pk_bf16_f32 v47, v52, v53
	global_load_dwordx4 v[48:51], v[60:61], off offset:256
	v_add_co_u32_e32 v52, vcc, s11, v158
	global_store_dwordx4 v[68:69], v[44:47], off sc0 sc1
	s_nop 0
	v_addc_co_u32_e32 v53, vcc, 0, v159, vcc
	s_mov_b32 s11, 0x58000
	s_waitcnt vmcnt(1)
	v_lshlrev_b32_e32 v44, 16, v48
	v_and_b32_e32 v45, 0xffff0000, v48
	v_lshlrev_b32_e32 v46, 16, v49
	v_and_b32_e32 v47, 0xffff0000, v49
	v_lshlrev_b32_e32 v48, 16, v50
	v_and_b32_e32 v49, 0xffff0000, v50
	v_lshlrev_b32_e32 v50, 16, v51
	v_and_b32_e32 v51, 0xffff0000, v51
	v_pk_fma_f32 v[42:43], v[42:43], v[122:123], v[46:47]
	v_pk_fma_f32 v[40:41], v[40:41], v[120:121], v[44:45]
	v_pk_fma_f32 v[44:45], v[34:35], v[118:119], v[50:51]
	v_pk_fma_f32 v[34:35], v[32:33], v[116:117], v[48:49]
	v_cvt_pk_bf16_f32 v32, v40, v41
	v_cvt_pk_bf16_f32 v33, v42, v43
	s_nop 0
	v_cvt_pk_bf16_f32 v34, v34, v35
	v_cvt_pk_bf16_f32 v35, v44, v45
	global_load_dwordx4 v[40:43], v[52:53], off
	v_lshl_add_u64 v[44:45], v[158:159], 0, s[20:21]
	global_store_dwordx4 v[60:61], v[32:35], off offset:256 sc0 sc1
	s_mov_b64 s[20:21], 0x58000
	s_waitcnt vmcnt(1)
	v_lshlrev_b32_e32 v32, 16, v40
	v_and_b32_e32 v33, 0xffff0000, v40
	v_lshlrev_b32_e32 v34, 16, v41
	v_and_b32_e32 v35, 0xffff0000, v41
	v_lshlrev_b32_e32 v40, 16, v42
	v_and_b32_e32 v41, 0xffff0000, v42
	v_lshlrev_b32_e32 v42, 16, v43
	v_and_b32_e32 v43, 0xffff0000, v43
	v_pk_fma_f32 v[34:35], v[38:39], v[138:139], v[34:35]
	v_pk_fma_f32 v[32:33], v[36:37], v[136:137], v[32:33]
	v_pk_fma_f32 v[36:37], v[30:31], v[134:135], v[42:43]
	v_pk_fma_f32 v[30:31], v[28:29], v[132:133], v[40:41]
	v_cvt_pk_bf16_f32 v28, v32, v33
	v_cvt_pk_bf16_f32 v29, v34, v35
	s_nop 0
	v_cvt_pk_bf16_f32 v30, v30, v31
	v_cvt_pk_bf16_f32 v31, v36, v37
	global_load_dwordx4 v[32:35], v[44:45], off offset:256
	v_add_co_u32_e32 v36, vcc, s11, v158
	global_store_dwordx4 v[52:53], v[28:31], off sc0 sc1
	s_nop 0
	v_addc_co_u32_e32 v37, vcc, 0, v159, vcc
	s_andn2_b64 vcc, exec, s[2:3]
	s_mov_b64 s[2:3], -1
	s_waitcnt vmcnt(1)
	v_lshlrev_b32_e32 v28, 16, v32
	v_and_b32_e32 v29, 0xffff0000, v32
	v_lshlrev_b32_e32 v30, 16, v33
	v_and_b32_e32 v31, 0xffff0000, v33
	v_lshlrev_b32_e32 v32, 16, v34
	v_and_b32_e32 v33, 0xffff0000, v34
	v_lshlrev_b32_e32 v34, 16, v35
	v_and_b32_e32 v35, 0xffff0000, v35
	v_pk_fma_f32 v[26:27], v[26:27], v[122:123], v[30:31]
	v_pk_fma_f32 v[24:25], v[24:25], v[120:121], v[28:29]
	v_pk_fma_f32 v[28:29], v[18:19], v[118:119], v[34:35]
	v_pk_fma_f32 v[18:19], v[16:17], v[116:117], v[32:33]
	v_cvt_pk_bf16_f32 v16, v24, v25
	v_cvt_pk_bf16_f32 v17, v26, v27
	s_nop 0
	v_cvt_pk_bf16_f32 v18, v18, v19
	v_cvt_pk_bf16_f32 v19, v28, v29
	global_load_dwordx4 v[24:27], v[36:37], off
	v_lshl_add_u64 v[28:29], v[158:159], 0, s[20:21]
	global_store_dwordx4 v[44:45], v[16:19], off offset:256 sc0 sc1
	s_waitcnt vmcnt(1)
	s_nop 0
	v_lshlrev_b32_e32 v16, 16, v24
	v_and_b32_e32 v17, 0xffff0000, v24
	v_lshlrev_b32_e32 v18, 16, v25
	v_and_b32_e32 v19, 0xffff0000, v25
	v_lshlrev_b32_e32 v24, 16, v26
	v_and_b32_e32 v25, 0xffff0000, v26
	v_lshlrev_b32_e32 v26, 16, v27
	v_and_b32_e32 v27, 0xffff0000, v27
	v_pk_fma_f32 v[18:19], v[22:23], v[138:139], v[18:19]
	v_pk_fma_f32 v[16:17], v[20:21], v[136:137], v[16:17]
	v_pk_fma_f32 v[20:21], v[14:15], v[134:135], v[26:27]
	v_pk_fma_f32 v[14:15], v[12:13], v[132:133], v[24:25]
	v_cvt_pk_bf16_f32 v12, v16, v17
	v_cvt_pk_bf16_f32 v13, v18, v19
	s_nop 0
	v_cvt_pk_bf16_f32 v14, v14, v15
	v_cvt_pk_bf16_f32 v15, v20, v21
	global_load_dwordx4 v[16:19], v[28:29], off offset:256
	s_nop 0
	global_store_dwordx4 v[36:37], v[12:15], off sc0 sc1
	s_waitcnt vmcnt(1)
	s_nop 0
	v_lshlrev_b32_e32 v12, 16, v16
	v_and_b32_e32 v13, 0xffff0000, v16
	v_lshlrev_b32_e32 v14, 16, v17
	v_and_b32_e32 v15, 0xffff0000, v17
	v_lshlrev_b32_e32 v16, 16, v18
	v_and_b32_e32 v17, 0xffff0000, v18
	v_lshlrev_b32_e32 v18, 16, v19
	v_and_b32_e32 v19, 0xffff0000, v19
	v_pk_fma_f32 v[8:9], v[8:9], v[120:121], v[12:13]
	v_pk_fma_f32 v[12:13], v[6:7], v[118:119], v[18:19]
	v_pk_fma_f32 v[6:7], v[4:5], v[116:117], v[16:17]
	v_pk_fma_f32 v[10:11], v[10:11], v[122:123], v[14:15]
	v_cvt_pk_bf16_f32 v4, v8, v9
	s_nop 0
	v_cvt_pk_bf16_f32 v5, v10, v11
	v_cvt_pk_bf16_f32 v6, v6, v7
	v_cvt_pk_bf16_f32 v7, v12, v13
	global_store_dwordx4 v[28:29], v[4:7], off offset:256 sc0 sc1
	s_cbranch_vccnz .LBB0_3160
	s_andn2_b64 vcc, exec, s[4:5]
	s_cbranch_vccnz .LBB0_3159
	s_barrier
	s_branch .LBB0_3159

; __device__ __forceinline__ unsigned cvt_pk_bf16(float lo, float hi) { unsigned r; asm volatile("v_cvt_pk_bf16_f32 %0, %1, %2" : "=v"(r) : "v"(lo), "v"(hi)); return r; }
;     __device__ __forceinline__ void operator()(const f32x4 (&acc)[2][2][4][2], const Unit& u, int wr, int wc, int fr, int fq) const {
;         const int row0 = u.pm * BM + wr * 64 + fr, col0 = (u.pn & 3) * BM + wc * 32 + 8 * fq;
; #pragma unroll
;         for (int ai = 0; ai < 2; ++ai)
; #pragma unroll
;             for (int m = 0; m < 4; ++m) { bf16_t* rowp = Yb + (size_t)(row0 + ai * HALF + m * 16) * 1024 + col0;
; #pragma unroll
;                 for (int bj = 0; bj < 2; ++bj) { const f32x4 v0 = acc[ai][bj][m][0], v1 = acc[ai][bj][m][1];
;                     u32x4 w; w.x = cvt_pk_bf16(v0[0], v0[1]); w.y = cvt_pk_bf16(v0[2], v0[3]); w.z = cvt_pk_bf16(v1[0], v1[1]); w.w = cvt_pk_bf16(v1[2], v1[3]);
;                     *(u32x4*)(rowp + bj * HALF) = w; } }
.LBB0_3874:
	v_lshl_add_u32 v150, s18, 8, v1
	s_lshl_b32 s9, s63, 8
	s_and_b32 s9, s9, 0x300
	v_ashrrev_i32_e32 v151, 31, v150
	v_or_b32_e32 v0, s9, v147
	v_lshlrev_b64 v[144:145], 11, v[150:151]
	v_lshl_add_u64 v[144:145], s[4:5], 0, v[144:145]
	v_lshlrev_b32_e32 v2, 1, v0
	v_lshl_add_u64 v[144:145], v[144:145], 0, v[2:3]
	v_cvt_pk_bf16_f32 v128, v128, v129
	v_cvt_pk_bf16_f32 v129, v130, v131
	v_cvt_pk_bf16_f32 v130, v124, v125
	v_cvt_pk_bf16_f32 v131, v126, v127
	global_store_dwordx4 v[144:145], v[128:131], off sc0 sc1
	v_cvt_pk_bf16_f32 v116, v116, v117
	v_cvt_pk_bf16_f32 v117, v118, v119
	v_cvt_pk_bf16_f32 v118, v108, v109
	v_or_b32_e32 v108, 16, v150
	v_ashrrev_i32_e32 v109, 31, v108
	v_lshlrev_b64 v[108:109], 11, v[108:109]
	v_lshl_add_u64 v[108:109], s[4:5], 0, v[108:109]
	v_cvt_pk_bf16_f32 v119, v110, v111
	global_store_dwordx4 v[144:145], v[116:119], off offset:256 sc0 sc1
	s_mov_b32 s9, 0x40000
	s_mov_b64 s[20:21], 0x40000
	v_lshl_add_u64 v[116:117], v[108:109], 0, v[2:3]
	v_cvt_pk_bf16_f32 v108, v120, v121
	v_cvt_pk_bf16_f32 v109, v122, v123
	v_cvt_pk_bf16_f32 v110, v112, v113
	v_cvt_pk_bf16_f32 v111, v114, v115
	global_store_dwordx4 v[116:117], v[108:111], off sc0 sc1
	v_cvt_pk_bf16_f32 v100, v100, v101
	v_cvt_pk_bf16_f32 v101, v102, v103
	v_cvt_pk_bf16_f32 v102, v92, v93
	v_or_b32_e32 v92, 32, v150
	v_ashrrev_i32_e32 v93, 31, v92
	v_lshlrev_b64 v[92:93], 11, v[92:93]
	v_lshl_add_u64 v[92:93], s[4:5], 0, v[92:93]
	v_cvt_pk_bf16_f32 v103, v94, v95
	global_store_dwordx4 v[116:117], v[100:103], off offset:256 sc0 sc1
	s_nop 1
	v_lshl_add_u64 v[100:101], v[92:93], 0, v[2:3]
	v_cvt_pk_bf16_f32 v92, v104, v105
	v_cvt_pk_bf16_f32 v93, v106, v107
	v_cvt_pk_bf16_f32 v94, v96, v97
	v_cvt_pk_bf16_f32 v95, v98, v99
	global_store_dwordx4 v[100:101], v[92:95], off sc0 sc1
	v_cvt_pk_bf16_f32 v84, v84, v85
	v_cvt_pk_bf16_f32 v85, v86, v87
	v_cvt_pk_bf16_f32 v86, v76, v77
	v_or_b32_e32 v76, 48, v150
	v_ashrrev_i32_e32 v77, 31, v76
	v_lshlrev_b64 v[76:77], 11, v[76:77]
	v_lshl_add_u64 v[76:77], s[4:5], 0, v[76:77]
	v_cvt_pk_bf16_f32 v87, v78, v79
	global_store_dwordx4 v[100:101], v[84:87], off offset:256 sc0 sc1
	s_nop 1
	v_lshl_add_u64 v[84:85], v[76:77], 0, v[2:3]
	v_cvt_pk_bf16_f32 v76, v88, v89
	v_cvt_pk_bf16_f32 v77, v90, v91
	v_cvt_pk_bf16_f32 v78, v80, v81
	v_cvt_pk_bf16_f32 v79, v82, v83
	global_store_dwordx4 v[84:85], v[76:79], off sc0 sc1
	v_cvt_pk_bf16_f32 v72, v72, v73
	v_cvt_pk_bf16_f32 v73, v74, v75
	v_cvt_pk_bf16_f32 v74, v68, v69
	v_cvt_pk_bf16_f32 v75, v70, v71
	global_store_dwordx4 v[84:85], v[72:75], off offset:256 sc0 sc1
	v_cvt_pk_bf16_f32 v64, v64, v65
	v_cvt_pk_bf16_f32 v65, v66, v67
	v_cvt_pk_bf16_f32 v66, v60, v61
	v_add_co_u32_e32 v60, vcc, s9, v144
	v_lshl_add_u64 v[68:69], v[144:145], 0, s[20:21]
	s_nop 0
	v_addc_co_u32_e32 v61, vcc, 0, v145, vcc
	s_mov_b32 s9, 0x48000
	v_cvt_pk_bf16_f32 v67, v62, v63
	global_store_dwordx4 v[60:61], v[64:67], off sc0 sc1
	v_cvt_pk_bf16_f32 v52, v52, v53
	v_cvt_pk_bf16_f32 v53, v54, v55
	v_cvt_pk_bf16_f32 v54, v44, v45
	v_cvt_pk_bf16_f32 v55, v46, v47
	global_store_dwordx4 v[68:69], v[52:55], off offset:256 sc0 sc1
	s_mov_b64 s[20:21], 0x48000
	v_cvt_pk_bf16_f32 v44, v56, v57
	v_cvt_pk_bf16_f32 v45, v58, v59
	v_cvt_pk_bf16_f32 v46, v48, v49
	v_add_co_u32_e32 v48, vcc, s9, v144
	v_lshl_add_u64 v[52:53], v[144:145], 0, s[20:21]
	s_nop 0
	v_addc_co_u32_e32 v49, vcc, 0, v145, vcc
	s_mov_b32 s9, 0x50000
	v_cvt_pk_bf16_f32 v47, v50, v51
	global_store_dwordx4 v[48:49], v[44:47], off sc0 sc1
	v_cvt_pk_bf16_f32 v36, v36, v37
	v_cvt_pk_bf16_f32 v37, v38, v39
	v_cvt_pk_bf16_f32 v38, v28, v29
	v_cvt_pk_bf16_f32 v39, v30, v31
	global_store_dwordx4 v[52:53], v[36:39], off offset:256 sc0 sc1
	s_mov_b64 s[20:21], 0x50000
	v_cvt_pk_bf16_f32 v28, v40, v41
	v_cvt_pk_bf16_f32 v29, v42, v43
	v_cvt_pk_bf16_f32 v30, v32, v33
	v_add_co_u32_e32 v32, vcc, s9, v144
	v_lshl_add_u64 v[36:37], v[144:145], 0, s[20:21]
	s_nop 0
	v_addc_co_u32_e32 v33, vcc, 0, v145, vcc
	s_mov_b32 s9, 0x58000
	v_cvt_pk_bf16_f32 v31, v34, v35
	global_store_dwordx4 v[32:33], v[28:31], off sc0 sc1
	v_cvt_pk_bf16_f32 v20, v20, v21
	v_cvt_pk_bf16_f32 v21, v22, v23
	v_cvt_pk_bf16_f32 v22, v12, v13
	v_cvt_pk_bf16_f32 v23, v14, v15
	global_store_dwordx4 v[36:37], v[20:23], off offset:256 sc0 sc1
	v_cvt_pk_bf16_f32 v12, v24, v25
	v_cvt_pk_bf16_f32 v13, v26, v27
	v_cvt_pk_bf16_f32 v14, v16, v17
	v_add_co_u32_e32 v16, vcc, s9, v144
	s_mov_b64 s[20:21], 0x58000
	s_nop 0
	v_addc_co_u32_e32 v17, vcc, 0, v145, vcc
	v_lshl_add_u64 v[20:21], v[144:145], 0, s[20:21]
	s_andn2_b64 vcc, exec, s[12:13]
	s_mov_b64 s[12:13], -1
	v_cvt_pk_bf16_f32 v15, v18, v19
	global_store_dwordx4 v[16:17], v[12:15], off sc0 sc1
	v_cvt_pk_bf16_f32 v8, v8, v9
	v_cvt_pk_bf16_f32 v9, v10, v11
	v_cvt_pk_bf16_f32 v10, v4, v5
	v_cvt_pk_bf16_f32 v11, v6, v7
	global_store_dwordx4 v[20:21], v[8:11], off offset:256 sc0 sc1
	s_cbranch_vccnz .LBB0_3867
	s_andn2_b64 vcc, exec, s[2:3]
	s_cbranch_vccnz .LBB0_3866
	s_barrier
	s_branch .LBB0_3866
